# first MoE unit's weight tiles requested during the grid barrier wait (waves 1..7)
# speedup vs baseline: 1.0030x; 1.0030x over previous
; #define GAS __attribute__((address_space(1)))
; #define LAS __attribute__((address_space(3)))
; __device__ __forceinline__ void xcd_barrier(const XcdBarrier& b) {
;     asm volatile("s_waitcnt vmcnt(0)" ::: "memory");
;     __syncthreads();
;     if (threadIdx.x == 0) {
;         unsigned* bar = b.bar;
;         __builtin_amdgcn_s_waitcnt(0);
;         unsigned nloc = b.st[0], nx = b.st[1];
;         if (nloc == 0u) { xcd_barrier_complete(bar, b.x, nloc, nx); b.st[0] = nloc; b.st[1] = nx; }
;     ...
;         const int xcd = vb & 7, idx = vb >> 3; const int e = xcd * 8 + idx / NSLAB, slab = idx % NSLAB;
;         const int M = __builtin_amdgcn_readfirstlane(lc[LC_CNT / 4 + e]), row0 = __builtin_amdgcn_readfirstlane(lc[LC_PSTART / 4 + e]);
;         const size_t wuo = (MODE == 0) ? ((size_t)(l * NEXP + e) * D * DEXP + slab * 64) * 4 : ((size_t)(l * NEXP + e) * DEXP * D + slab * 128 + 64 * half) * 4;
;         const __amdgpu_buffer_rsrc_t wrs = __builtin_amdgcn_make_buffer_rsrc((void*)(wmat + wuo), 0, KD * LDW * 4, 0x00020000);
;         const __amdgpu_buffer_rsrc_t xrs = __builtin_amdgcn_make_buffer_rsrc((MODE == 0) ? (void*)(ws + WS_U) : (void*)((const GAS char*)(ws + WS_HID) + (size_t)row0 * LDX * 2), 0, 0x7fffffff, 0x00020000);
;         const int* el = (const int*)(ws + WS_ELIST) + (size_t)e * T;
;         for (int rp = 0; rp < M; rp += 384) {
;             unsigned xso[6];
; #pragma unroll
;             for (int i = 0; i < 6; ++i) { int tok = rp + wave * 48 + 8 * i + (lane >> 3); tok = min(tok, M - 1); if (VAR == 5) tok &= 15; if (MODE == 0) tok = el[tok]; xso[i] = (unsigned)(tok * LDX * 2 + (lane & 7) * 16); }
;             LAS unsigned char* xw = lds + MS_XOFF + wave * MS_XWAVE; const int xwo = (lane >> 3) * 128 + (((lane & 7) ^ ((lane >> 4) & 3)) << 4);
;             const LAS unsigned char* xr = lds + MS_XOFF + wave * MS_XWAVE + tk * 128 + ((q ^ rd_g) << 4);
;             f32x4 acc[3][8];
; #pragma unroll
;             for (int mt = 0; mt < 3; ++mt)
; #pragma unroll
;                 for (int j = 0; j < 8; ++j) acc[mt][j] = (f32x4){0.f, 0.f, 0.f, 0.f};
;             f32x4 wr[2][4];
;             bf16x8 xs[6];
.LBB0_1658:
	s_mov_b32 s67, 0
	v_readlane_b32 s0, v255, 32
	s_add_i32 s0, s0, 9
	s_cmp_ge_i32 s0, s77
	s_cbranch_scc1 .LBB0_1708
	s_waitcnt vmcnt(0)
	s_waitcnt lgkmcnt(0)
	s_barrier
	v_readfirstlane_b32 s88, v0
	s_lshr_b32 s88, s88, 6
	s_cmp_eq_u32 s88, 0
	s_cbranch_scc1 .Lpfk_end
	s_cmpk_gt_i32 s72, 0x1ff
	s_cbranch_scc1 .Lpfk_end
	s_and_b32 s81, s88, 1
	s_lshl_b32 s81, s81, 3
	s_add_i32 s81, s81, 0xe8
	s_load_dwordx2 s[70:71], s[74:75], s81
	v_readlane_b32 s82, v255, 30
	s_lshl_b32 s82, s82, 6
	s_and_b32 s84, s72, 7
	s_lshl_b32 s84, s84, 3
	s_lshr_b32 s85, s72, 6
	s_add_i32 s84, s84, s85
	s_add_i32 s84, s84, s82
	s_lshr_b32 s85, s72, 3
	s_and_b32 s85, s85, 7
	s_lshl_b32 s85, s85, 8
	s_lshr_b32 s86, s84, 10
	s_lshl_b32 s84, s84, 22
	s_or_b32 s84, s84, s85
	s_waitcnt lgkmcnt(0)
	s_add_u32 s84, s70, s84
	s_addc_u32 s85, s71, s86
	s_and_b32 s85, s85, 0xffff
	s_mov_b32 s86, 0x7ffffff0
	s_mov_b32 s87, 0x20000
	v_and_b32_e32 v250, 15, v0
	v_lshlrev_b32_e32 v250, 4, v250
	v_bfe_u32 v251, v0, 4, 2
	s_lshr_b32 s81, s88, 1
	s_lshl_b32 s81, s81, 2
	v_add_u32_e32 v251, s81, v251
	v_lshl_or_b32 v250, v251, 13, v250
	v_or_b32_e32 v251, 0x800, v250
	v_or_b32_e32 v252, 0x1000, v250
	v_or_b32_e32 v253, 0x1800, v250
	buffer_load_dwordx4 v[26:29], v250, s[84:87], 0 offen nt
	buffer_load_dwordx4 v[30:33], v251, s[84:87], 0 offen nt
	buffer_load_dwordx4 v[34:37], v252, s[84:87], 0 offen nt
	buffer_load_dwordx4 v[38:41], v253, s[84:87], 0 offen nt
	s_mov_b32 s81, 0x20000
	buffer_load_dwordx4 v[74:77], v250, s[84:87], s81 offen nt
	buffer_load_dwordx4 v[78:81], v251, s[84:87], s81 offen nt
	buffer_load_dwordx4 v[82:85], v252, s[84:87], s81 offen nt
	buffer_load_dwordx4 v[86:89], v253, s[84:87], s81 offen nt
	s_mov_b32 s81, 0x40000
	buffer_load_dwordx4 v[96:99], v250, s[84:87], s81 offen nt
	buffer_load_dwordx4 v[100:103], v251, s[84:87], s81 offen nt
	buffer_load_dwordx4 v[104:107], v252, s[84:87], s81 offen nt
	buffer_load_dwordx4 v[108:111], v253, s[84:87], s81 offen nt
	s_mov_b32 s67, 1
.Lpfk_end:
	s_mov_b64 s[4:5], exec
	v_readlane_b32 s2, v255, 21
	v_readlane_b32 s3, v255, 22
	s_and_b64 s[2:3], s[4:5], s[2:3]
	s_mov_b64 exec, s[2:3]
	s_cbranch_execz .LBB0_1707
	v_readlane_b32 s1, v254, 0
	s_waitcnt vmcnt(0) expcnt(0) lgkmcnt(0)
	s_nop 0
	v_mov_b32_e32 v2, s1
	ds_read_b32 v4, v2
	ds_read_b32 v2, v2 offset:4
	s_waitcnt lgkmcnt(1)
	v_cmp_ne_u32_e32 vcc, 0, v4
	s_cbranch_vccnz .LBB0_1675
	s_load_dwordx2 s[2:3], s[78:79], 0x0
	s_load_dword s1, s[78:79], 0x8
	s_mov_b32 s7, 1
	s_waitcnt lgkmcnt(0)
	s_mul_i32 s2, s3, s2
	s_mul_i32 s1, s2, s1
	s_branch .LBB0_1663

;     ...
;     for (int vb = bid; vb < NEXP * NSLAB; vb += G) {
;         const int xcd = vb & 7, idx = vb >> 3; const int e = xcd * 8 + idx / NSLAB, slab = idx % NSLAB;
;         const int M = __builtin_amdgcn_readfirstlane(lc[LC_CNT / 4 + e]), row0 = __builtin_amdgcn_readfirstlane(lc[LC_PSTART / 4 + e]);
.LBB0_1715:
	s_mov_b32 s67, 0
	s_add_i32 s3, s3, s2
	s_cmpk_gt_i32 s3, 0x1ff
	s_cbranch_scc1 .LBB0_1727

; #define LAS __attribute__((address_space(3)))
; #define MS_WLOAD(set, t) do { _Pragma("unroll") for (int r_ = 0; r_ < 4; ++r_) wr[set][r_] = __builtin_bit_cast(f32x4, __builtin_amdgcn_raw_buffer_load_b128(wrs, (int)wvo + r_ * LDW * 4, MS_CL(t) * (64 * LDW * 4), 0)); } while (0)
; #define MS_WCOMMIT(set, bufi) do { LAS unsigned char* wb_ = lds + (bufi) * MS_TILE; _Pragma("unroll") for (int i_ = 0; i_ < 4; ++i_) { \
;             u32x2 p_; p_.x = pk2(wr[set][0][i_], wr[set][1][i_]); p_.y = pk2(wr[set][2][i_], wr[set][3][i_]); \
;             *(LAS u32x2*)(wb_ + ((i_ < 2) ? lw0 : lw1) + i_ * 128) = p_; } } while (0)
; #define MS_XSLOAD(t) do { _Pragma("unroll") for (int i_ = 0; i_ < 6; ++i_) xs[i_] = __builtin_bit_cast(bf16x8, __builtin_amdgcn_raw_buffer_load_b128(xrs, (int)xso[i_], MS_CL(t) * 128, 0)); } while (0)
; #define MS_XSWRITE(bufi) do { _Pragma("unroll") for (int i_ = 0; i_ < 6; ++i_) *(LAS bf16x8*)(xw + (bufi) * MS_XBUF + i_ * 1024 + ((i_ & 1) ? (xwo ^ 64) : xwo)) = xs[i_]; } while (0)
;     ...
;             for (int i = 0; i < 6; ++i) { int tok = rp + wave * 48 + 8 * i + (lane >> 3); tok = min(tok, M - 1); if (VAR == 5) tok &= 15; if (MODE == 0) tok = el[tok]; xso[i] = (unsigned)(tok * LDX * 2 + (lane & 7) * 16); }
;             LAS unsigned char* xw = lds + MS_XOFF + wave * MS_XWAVE; const int xwo = (lane >> 3) * 128 + (((lane & 7) ^ ((lane >> 4) & 3)) << 4);
;             const LAS unsigned char* xr = lds + MS_XOFF + wave * MS_XWAVE + tk * 128 + ((q ^ rd_g) << 4);
;             f32x4 acc[3][8];
; #pragma unroll
;             for (int mt = 0; mt < 3; ++mt)
; #pragma unroll
;                 for (int j = 0; j < 8; ++j) acc[mt][j] = (f32x4){0.f, 0.f, 0.f, 0.f};
;             f32x4 wr[2][4];
;             bf16x8 xs[6];
;     ...
;             const LAS unsigned char* xr1 = lds + MS_XOFF + wave * MS_XWAVE + tk * 128 + (((4 + q) ^ rd_g) << 4);
;             __syncthreads();
;             MS_XSLOAD(0); MS_WLOAD(0, 0); MS_WLOAD(1, 1);
;             MS_WCOMMIT(0, 0); MS_WLOAD(0, 2);
;             MS_XSWRITE(0); MS_XSLOAD(1);
;             __syncthreads();
.Lxk_nel:
	s_cmp_eq_u32 s83, 1
	s_cbranch_scc1 .Lxk_fast
	v_add_u32_e32 v4, s31, v162
	v_min_i32_e32 v2, s30, v4
	v_ashrrev_i32_e32 v3, 31, v2
	v_lshl_add_u64 v[2:3], v[2:3], 2, s[40:41]
	global_load_dword v182, v[2:3], off
	v_or_b32_e32 v2, 8, v4
	v_min_i32_e32 v2, s30, v2
	v_ashrrev_i32_e32 v3, 31, v2
	v_lshl_add_u64 v[2:3], v[2:3], 2, s[40:41]
	global_load_dword v183, v[2:3], off
	v_add_u32_e32 v2, 0x80, v4
	v_min_i32_e32 v2, s30, v2
	v_ashrrev_i32_e32 v3, 31, v2
	v_lshl_add_u64 v[2:3], v[2:3], 2, s[40:41]
	global_load_dword v184, v[2:3], off
	v_add_u32_e32 v2, 0x88, v4
	v_min_i32_e32 v2, s30, v2
	v_ashrrev_i32_e32 v3, 31, v2
	v_lshl_add_u64 v[2:3], v[2:3], 2, s[40:41]
	global_load_dword v185, v[2:3], off
	v_add_u32_e32 v2, 0x100, v4
	v_min_i32_e32 v2, s30, v2
	v_ashrrev_i32_e32 v3, 31, v2
	v_lshl_add_u64 v[2:3], v[2:3], 2, s[40:41]
	global_load_dword v186, v[2:3], off
	v_add_u32_e32 v2, 0x108, v4
	v_min_i32_e32 v2, s30, v2
	v_ashrrev_i32_e32 v3, 31, v2
	v_lshl_add_u64 v[2:3], v[2:3], 2, s[40:41]
	global_load_dword v187, v[2:3], off
	v_add_u32_e32 v188, 0, v161
	v_add_u32_e32 v189, s27, v172
	s_mov_b32 s0, -2
	s_barrier
	s_waitcnt vmcnt(0)
	v_lshl_or_b32 v182, v182, 12, v163
	v_lshl_or_b32 v183, v183, 12, v163
	v_lshl_or_b32 v184, v184, 12, v163
	v_lshl_or_b32 v185, v185, 12, v163
	v_lshl_or_b32 v186, v186, 12, v163
	v_lshl_or_b32 v187, v187, 12, v163
	buffer_load_dwordx4 v[2:5], v182, s[4:7], 0 offen
	buffer_load_dwordx4 v[6:9], v183, s[4:7], 0 offen
	buffer_load_dwordx4 v[10:13], v184, s[4:7], 0 offen
	buffer_load_dwordx4 v[14:17], v185, s[4:7], 0 offen
	buffer_load_dwordx4 v[18:21], v186, s[4:7], 0 offen
	buffer_load_dwordx4 v[22:25], v187, s[4:7], 0 offen
	s_cmp_eq_u32 s67, 0
	s_cbranch_scc1 .Lpfk_ld01
	s_waitcnt vmcnt(0)
	s_branch .Lpfk_w01
.Lpfk_ld01:
	buffer_load_dwordx4 v[26:29], v160, s[8:11], 0 offen nt
	buffer_load_dwordx4 v[30:33], v90, s[8:11], 0 offen nt
	buffer_load_dwordx4 v[34:37], v178, s[8:11], 0 offen nt
	buffer_load_dwordx4 v[38:41], v179, s[8:11], 0 offen nt
	buffer_load_dwordx4 v[74:77], v160, s[8:11], s11 offen nt
	buffer_load_dwordx4 v[78:81], v90, s[8:11], s11 offen nt
	buffer_load_dwordx4 v[82:85], v178, s[8:11], s11 offen nt
	buffer_load_dwordx4 v[86:89], v179, s[8:11], s11 offen nt
.Lpfk_w01:
	s_waitcnt vmcnt(6)
	v_cvt_pk_bf16_f32 v42, v26, v30
	v_cvt_pk_bf16_f32 v26, v27, v31
	s_waitcnt vmcnt(4)
	v_cvt_pk_bf16_f32 v43, v34, v38
	v_cvt_pk_bf16_f32 v27, v35, v39
	ds_write2_b64 v188, v[42:43], v[26:27] offset1:16
	v_cvt_pk_bf16_f32 v26, v28, v32
	v_cvt_pk_bf16_f32 v27, v36, v40
	v_cvt_pk_bf16_f32 v28, v29, v33
	v_cvt_pk_bf16_f32 v29, v37, v41
	ds_write2_b64 v180, v[26:27], v[28:29] offset0:32 offset1:48
	s_cmp_lg_u32 s67, 0
	s_cbranch_scc1 .Lpfk_w2
	buffer_load_dwordx4 v[96:99], v160, s[8:11], s22 offen nt
	buffer_load_dwordx4 v[100:103], v90, s[8:11], s22 offen nt
	buffer_load_dwordx4 v[104:107], v178, s[8:11], s22 offen nt
	buffer_load_dwordx4 v[108:111], v179, s[8:11], s22 offen nt
.Lpfk_w2:
	ds_write_b128 v189, v[2:5] offset:32768
	ds_write_b128 v181, v[6:9] offset:33792
	ds_write_b128 v189, v[10:13] offset:34816
	ds_write_b128 v181, v[14:17] offset:35840
	ds_write_b128 v189, v[18:21] offset:36864
	ds_write_b128 v181, v[22:25] offset:37888
	buffer_load_dwordx4 v[132:135], v182, s[4:7], s92 offen
	buffer_load_dwordx4 v[124:127], v183, s[4:7], s92 offen
	buffer_load_dwordx4 v[140:143], v184, s[4:7], s92 offen
	buffer_load_dwordx4 v[144:147], v185, s[4:7], s92 offen
	buffer_load_dwordx4 v[128:131], v186, s[4:7], s92 offen
	buffer_load_dwordx4 v[136:139], v187, s[4:7], s92 offen
	v_mov_b32_e32 v2, 0
	v_mov_b32_e32 v3, v2
	v_mov_b32_e32 v4, v2
	v_mov_b32_e32 v5, v2
	v_mov_b32_e32 v10, v2
	v_mov_b32_e32 v11, v2
	v_mov_b32_e32 v12, v2
	v_mov_b32_e32 v13, v2
	v_mov_b32_e32 v18, v2
	v_mov_b32_e32 v19, v2
	v_mov_b32_e32 v20, v2
	v_mov_b32_e32 v21, v2
	v_mov_b32_e32 v26, v2
	v_mov_b32_e32 v27, v2
	v_mov_b32_e32 v28, v2
	v_mov_b32_e32 v29, v2
	v_mov_b32_e32 v6, v2
	v_mov_b32_e32 v7, v2
	v_mov_b32_e32 v8, v2
	v_mov_b32_e32 v9, v2
	v_mov_b32_e32 v14, v2
	v_mov_b32_e32 v15, v2
	v_mov_b32_e32 v16, v2
	v_mov_b32_e32 v17, v2
	v_mov_b32_e32 v22, v2
	v_mov_b32_e32 v23, v2
	v_mov_b32_e32 v24, v2
	v_mov_b32_e32 v25, v2
	v_mov_b32_e32 v30, v2
	v_mov_b32_e32 v31, v2
	v_mov_b32_e32 v32, v2
	v_mov_b32_e32 v33, v2
	v_mov_b32_e32 v34, v2
	v_mov_b32_e32 v35, v2
	v_mov_b32_e32 v36, v2
	v_mov_b32_e32 v37, v2
	v_mov_b32_e32 v42, v2
	v_mov_b32_e32 v43, v2
	v_mov_b32_e32 v44, v2
	v_mov_b32_e32 v45, v2
	v_mov_b32_e32 v50, v2
	v_mov_b32_e32 v51, v2
	v_mov_b32_e32 v52, v2
	v_mov_b32_e32 v53, v2
	v_mov_b32_e32 v58, v2
	v_mov_b32_e32 v59, v2
	v_mov_b32_e32 v60, v2
	v_mov_b32_e32 v61, v2
	v_mov_b32_e32 v38, v2
	v_mov_b32_e32 v39, v2
	v_mov_b32_e32 v40, v2
	v_mov_b32_e32 v41, v2
	v_mov_b32_e32 v46, v2
	v_mov_b32_e32 v47, v2
	v_mov_b32_e32 v48, v2
	v_mov_b32_e32 v49, v2
	v_mov_b32_e32 v54, v2
	v_mov_b32_e32 v55, v2
	v_mov_b32_e32 v56, v2
	v_mov_b32_e32 v57, v2
	v_mov_b32_e32 v62, v2
	v_mov_b32_e32 v63, v2
	v_mov_b32_e32 v64, v2
	v_mov_b32_e32 v65, v2
	v_mov_b32_e32 v66, v2
	v_mov_b32_e32 v67, v2
	v_mov_b32_e32 v68, v2
	v_mov_b32_e32 v69, v2
	v_mov_b32_e32 v92, v2
	v_mov_b32_e32 v93, v2
	v_mov_b32_e32 v94, v2
	v_mov_b32_e32 v95, v2
	v_mov_b32_e32 v116, v2
	v_mov_b32_e32 v117, v2
	v_mov_b32_e32 v118, v2
	v_mov_b32_e32 v119, v2
	v_mov_b32_e32 v148, v2
	v_mov_b32_e32 v149, v2
	v_mov_b32_e32 v150, v2
	v_mov_b32_e32 v151, v2
	v_mov_b32_e32 v70, v2
	v_mov_b32_e32 v71, v2
	v_mov_b32_e32 v72, v2
	v_mov_b32_e32 v73, v2
	v_mov_b32_e32 v112, v2
	v_mov_b32_e32 v113, v2
	v_mov_b32_e32 v114, v2
	v_mov_b32_e32 v115, v2
	v_mov_b32_e32 v120, v2
	v_mov_b32_e32 v121, v2
	v_mov_b32_e32 v122, v2
	v_mov_b32_e32 v123, v2
	v_mov_b32_e32 v152, v2
	v_mov_b32_e32 v153, v2
	v_mov_b32_e32 v154, v2
	v_mov_b32_e32 v155, v2
	s_waitcnt lgkmcnt(0)
	s_barrier
.Lxk_disp:
	s_mov_b32 s67, 0
	s_sub_i32 s81, s28, s31
	s_add_i32 s82, s80, 0x100
	s_cmp_gt_i32 s81, s82
	s_cbranch_scc1 .LBB0_1720
	s_cmp_eq_u32 s84, 0
	s_cbranch_scc1 .Lmoe_k_b
	s_add_i32 s81, s86, 1
	s_sub_i32 s81, s81, s87
	s_cmp_le_i32 s81, s82
	s_cbranch_scc1 .Lmoe_k_b

; #define GAS __attribute__((address_space(1)))
; #define LAS __attribute__((address_space(3)))
; __device__ __forceinline__ void xcd_barrier(const XcdBarrier& b) {
;     asm volatile("s_waitcnt vmcnt(0)" ::: "memory");
;     __syncthreads();
;     if (threadIdx.x == 0) {
;         unsigned* bar = b.bar;
;         __builtin_amdgcn_s_waitcnt(0);
;         unsigned nloc = b.st[0], nx = b.st[1];
;         if (nloc == 0u) { xcd_barrier_complete(bar, b.x, nloc, nx); b.st[0] = nloc; b.st[1] = nx; }
;     ...
;         const int xcd = vb & 7, idx = vb >> 3; const int e = xcd * 8 + idx / NSLAB, slab = idx % NSLAB;
;         const int M = __builtin_amdgcn_readfirstlane(lc[LC_CNT / 4 + e]), row0 = __builtin_amdgcn_readfirstlane(lc[LC_PSTART / 4 + e]);
;         const size_t wuo = (MODE == 0) ? ((size_t)(l * NEXP + e) * D * DEXP + slab * 64) * 4 : ((size_t)(l * NEXP + e) * DEXP * D + slab * 128 + 64 * half) * 4;
;         const __amdgpu_buffer_rsrc_t wrs = __builtin_amdgcn_make_buffer_rsrc((void*)(wmat + wuo), 0, KD * LDW * 4, 0x00020000);
;         const __amdgpu_buffer_rsrc_t xrs = __builtin_amdgcn_make_buffer_rsrc((MODE == 0) ? (void*)(ws + WS_U) : (void*)((const GAS char*)(ws + WS_HID) + (size_t)row0 * LDX * 2), 0, 0x7fffffff, 0x00020000);
;         const int* el = (const int*)(ws + WS_ELIST) + (size_t)e * T;
;         for (int rp = 0; rp < M; rp += 384) {
;             unsigned xso[6];
; #pragma unroll
;             for (int i = 0; i < 6; ++i) { int tok = rp + wave * 48 + 8 * i + (lane >> 3); tok = min(tok, M - 1); if (VAR == 5) tok &= 15; if (MODE == 0) tok = el[tok]; xso[i] = (unsigned)(tok * LDX * 2 + (lane & 7) * 16); }
;             LAS unsigned char* xw = lds + MS_XOFF + wave * MS_XWAVE; const int xwo = (lane >> 3) * 128 + (((lane & 7) ^ ((lane >> 4) & 3)) << 4);
;             const LAS unsigned char* xr = lds + MS_XOFF + wave * MS_XWAVE + tk * 128 + ((q ^ rd_g) << 4);
;             f32x4 acc[3][8];
; #pragma unroll
;             for (int mt = 0; mt < 3; ++mt)
; #pragma unroll
;                 for (int j = 0; j < 8; ++j) acc[mt][j] = (f32x4){0.f, 0.f, 0.f, 0.f};
;             f32x4 wr[2][4];
;             bf16x8 xs[6];
.LBB0_1727:
	s_mov_b32 s67, 0
	s_mov_b32 s10, 0x400000
	v_readlane_b32 s0, v255, 32
	s_add_i32 s0, s0, 10
	s_cmp_ge_i32 s0, s77
	s_cbranch_scc1 .LBB0_1777
	s_waitcnt vmcnt(0)
	s_barrier
	v_readfirstlane_b32 s88, v0
	s_lshr_b32 s88, s88, 6
	s_cmp_eq_u32 s88, 0
	s_cbranch_scc1 .Lpfl_end
	s_cmpk_gt_i32 s72, 0x3ff
	s_cbranch_scc1 .Lpfl_end
	s_load_dwordx2 s[70:71], s[74:75], 0xf8
	v_readlane_b32 s82, v255, 30
	s_lshl_b32 s82, s82, 6
	s_and_b32 s84, s72, 7
	s_lshl_b32 s84, s84, 3
	s_lshr_b32 s85, s72, 7
	s_add_i32 s84, s84, s85
	s_add_i32 s84, s84, s82
	s_lshr_b32 s85, s72, 3
	s_and_b32 s85, s85, 15
	s_lshl_b32 s85, s85, 9
	s_and_b32 s81, s88, 1
	s_lshl_b32 s81, s81, 8
	s_or_b32 s85, s85, s81
	s_lshr_b32 s86, s84, 10
	s_lshl_b32 s84, s84, 22
	s_or_b32 s84, s84, s85
	s_waitcnt lgkmcnt(0)
	s_add_u32 s84, s70, s84
	s_addc_u32 s85, s71, s86
	s_and_b32 s85, s85, 0xffff
	s_mov_b32 s86, 0x7ffffff0
	s_mov_b32 s87, 0x20000
	v_and_b32_e32 v250, 15, v0
	v_lshlrev_b32_e32 v250, 4, v250
	v_bfe_u32 v251, v0, 4, 2
	s_lshr_b32 s81, s88, 1
	s_lshl_b32 s81, s81, 2
	v_add_u32_e32 v251, s81, v251
	v_lshl_or_b32 v250, v251, 15, v250
	v_or_b32_e32 v251, 0x2000, v250
	v_or_b32_e32 v252, 0x4000, v250
	v_or_b32_e32 v253, 0x6000, v250
	buffer_load_dwordx4 v[52:55], v250, s[84:87], 0 offen nt
	buffer_load_dwordx4 v[56:59], v251, s[84:87], 0 offen nt
	buffer_load_dwordx4 v[60:63], v252, s[84:87], 0 offen nt
	buffer_load_dwordx4 v[64:67], v253, s[84:87], 0 offen nt
	s_mov_b32 s81, 0x80000
	buffer_load_dwordx4 v[120:123], v250, s[84:87], s81 offen nt
	buffer_load_dwordx4 v[128:131], v251, s[84:87], s81 offen nt
	buffer_load_dwordx4 v[124:127], v252, s[84:87], s81 offen nt
	buffer_load_dwordx4 v[132:135], v253, s[84:87], s81 offen nt
	s_mov_b32 s81, 0x100000
	buffer_load_dwordx4 v[136:139], v250, s[84:87], s81 offen nt
	buffer_load_dwordx4 v[140:143], v251, s[84:87], s81 offen nt
	buffer_load_dwordx4 v[144:147], v252, s[84:87], s81 offen nt
	buffer_load_dwordx4 v[148:151], v253, s[84:87], s81 offen nt
	s_mov_b32 s67, 1

; #define GAS __attribute__((address_space(1)))
;     ...
;     for (int vb = bid; vb < NEXP * NSLAB; vb += G) {
;         const int xcd = vb & 7, idx = vb >> 3; const int e = xcd * 8 + idx / NSLAB, slab = idx % NSLAB;
;         const int M = __builtin_amdgcn_readfirstlane(lc[LC_CNT / 4 + e]), row0 = __builtin_amdgcn_readfirstlane(lc[LC_PSTART / 4 + e]);
;         const size_t wuo = (MODE == 0) ? ((size_t)(l * NEXP + e) * D * DEXP + slab * 64) * 4 : ((size_t)(l * NEXP + e) * DEXP * D + slab * 128 + 64 * half) * 4;
;         const __amdgpu_buffer_rsrc_t wrs = __builtin_amdgcn_make_buffer_rsrc((void*)(wmat + wuo), 0, KD * LDW * 4, 0x00020000);
;         const __amdgpu_buffer_rsrc_t xrs = __builtin_amdgcn_make_buffer_rsrc((MODE == 0) ? (void*)(ws + WS_U) : (void*)((const GAS char*)(ws + WS_HID) + (size_t)row0 * LDX * 2), 0, 0x7fffffff, 0x00020000);
;         const int* el = (const int*)(ws + WS_ELIST) + (size_t)e * T;
;         for (int rp = 0; rp < M; rp += 384) {
.LBB0_1780:
	s_mov_b32 s67, 0
	s_add_i32 s1, s1, s0
	s_cmpk_gt_i32 s1, 0x3ff
	s_cbranch_scc1 .LBB0_1792

; #define LAS __attribute__((address_space(3)))
; #define MS_WLOAD(set, t) do { _Pragma("unroll") for (int r_ = 0; r_ < 4; ++r_) wr[set][r_] = __builtin_bit_cast(f32x4, __builtin_amdgcn_raw_buffer_load_b128(wrs, (int)wvo + r_ * LDW * 4, MS_CL(t) * (64 * LDW * 4), 0)); } while (0)
; #define MS_WCOMMIT(set, bufi) do { LAS unsigned char* wb_ = lds + (bufi) * MS_TILE; _Pragma("unroll") for (int i_ = 0; i_ < 4; ++i_) { \
;             u32x2 p_; p_.x = pk2(wr[set][0][i_], wr[set][1][i_]); p_.y = pk2(wr[set][2][i_], wr[set][3][i_]); \
;             *(LAS u32x2*)(wb_ + ((i_ < 2) ? lw0 : lw1) + i_ * 128) = p_; } } while (0)
; #define MS_XSLOAD(t) do { _Pragma("unroll") for (int i_ = 0; i_ < 6; ++i_) xs[i_] = __builtin_bit_cast(bf16x8, __builtin_amdgcn_raw_buffer_load_b128(xrs, (int)xso[i_], MS_CL(t) * 128, 0)); } while (0)
; #define MS_XSWRITE(bufi) do { _Pragma("unroll") for (int i_ = 0; i_ < 6; ++i_) *(LAS bf16x8*)(xw + (bufi) * MS_XBUF + i_ * 1024 + ((i_ & 1) ? (xwo ^ 64) : xwo)) = xs[i_]; } while (0)
;     ...
;             unsigned xso[6];
; #pragma unroll
;             for (int i = 0; i < 6; ++i) { int tok = rp + wave * 48 + 8 * i + (lane >> 3); tok = min(tok, M - 1); if (VAR == 5) tok &= 15; if (MODE == 0) tok = el[tok]; xso[i] = (unsigned)(tok * LDX * 2 + (lane & 7) * 16); }
;             LAS unsigned char* xw = lds + MS_XOFF + wave * MS_XWAVE; const int xwo = (lane >> 3) * 128 + (((lane & 7) ^ ((lane >> 4) & 3)) << 4);
;             const LAS unsigned char* xr = lds + MS_XOFF + wave * MS_XWAVE + tk * 128 + ((q ^ rd_g) << 4);
;             f32x4 acc[3][8];
; #pragma unroll
;             for (int mt = 0; mt < 3; ++mt)
; #pragma unroll
;                 for (int j = 0; j < 8; ++j) acc[mt][j] = (f32x4){0.f, 0.f, 0.f, 0.f};
;             f32x4 wr[2][4];
;             bf16x8 xs[6];
;     ...
;             const LAS unsigned char* xr1 = lds + MS_XOFF + wave * MS_XWAVE + tk * 128 + (((4 + q) ^ rd_g) << 4);
;             __syncthreads();
;             MS_XSLOAD(0); MS_WLOAD(0, 0); MS_WLOAD(1, 1);
;             MS_WCOMMIT(0, 0); MS_WLOAD(0, 2);
;             MS_XSWRITE(0); MS_XSLOAD(1);
;             __syncthreads();
.Lxl_sel:
	v_add_u32_e32 v240, s31, v162
	v_min_i32_e32 v241, s25, v240
	v_lshl_or_b32 v182, v241, 10, v163
	v_or_b32_e32 v241, 8, v240
	v_min_i32_e32 v241, s25, v241
	v_lshl_or_b32 v183, v241, 10, v163
	v_add_u32_e32 v241, 0x80, v240
	v_min_i32_e32 v241, s25, v241
	v_lshl_or_b32 v184, v241, 10, v163
	v_add_u32_e32 v241, 0x88, v240
	v_min_i32_e32 v241, s25, v241
	v_lshl_or_b32 v185, v241, 10, v163
	v_add_u32_e32 v241, 0x100, v240
	v_min_i32_e32 v241, s25, v241
	v_lshl_or_b32 v186, v241, 10, v163
	v_add_u32_e32 v241, 0x108, v240
	v_min_i32_e32 v241, s25, v241
	v_lshl_or_b32 v187, v241, 10, v163
	s_cmp_eq_u32 s83, 1
	s_cbranch_scc1 .Lxl_fast
	s_barrier
	s_cmp_lg_u32 s67, 0
	s_cbranch_scc1 .Lpfl_w0
	buffer_load_dwordx4 v[52:55], v160, s[8:11], 0 offen nt
	buffer_load_dwordx4 v[56:59], v90, s[8:11], 0 offen nt
	buffer_load_dwordx4 v[60:63], v178, s[8:11], 0 offen nt
	buffer_load_dwordx4 v[64:67], v179, s[8:11], 0 offen nt
.Lpfl_w0:
	buffer_load_dwordx4 v[68:71], v182, s[4:7], 0 offen
	buffer_load_dwordx4 v[72:75], v183, s[4:7], 0 offen
	buffer_load_dwordx4 v[76:79], v184, s[4:7], 0 offen
	buffer_load_dwordx4 v[80:83], v185, s[4:7], 0 offen
	buffer_load_dwordx4 v[84:87], v186, s[4:7], 0 offen
	buffer_load_dwordx4 v[96:99], v187, s[4:7], 0 offen
	s_cmp_lg_u32 s67, 0
	s_cbranch_scc1 .Lpfl_mv
	buffer_load_dwordx4 v[2:5], v160, s[8:11], s23 offen nt
	buffer_load_dwordx4 v[6:9], v178, s[8:11], s23 offen nt
	buffer_load_dwordx4 v[18:21], v160, s[8:11], s93 offen nt
	buffer_load_dwordx4 v[10:13], v90, s[8:11], s23 offen nt
	buffer_load_dwordx4 v[22:25], v90, s[8:11], s93 offen nt
	buffer_load_dwordx4 v[26:29], v178, s[8:11], s93 offen nt
	buffer_load_dwordx4 v[14:17], v179, s[8:11], s23 offen nt
	buffer_load_dwordx4 v[30:33], v179, s[8:11], s93 offen nt
	s_branch .Lpfl_w12
.Lpfl_mv:
	v_mov_b32_e32 v2, v120
	v_mov_b32_e32 v3, v121
	v_mov_b32_e32 v4, v122
	v_mov_b32_e32 v5, v123
	v_mov_b32_e32 v6, v124
	v_mov_b32_e32 v7, v125
	v_mov_b32_e32 v8, v126
	v_mov_b32_e32 v9, v127
	v_mov_b32_e32 v10, v128
	v_mov_b32_e32 v11, v129
	v_mov_b32_e32 v12, v130
	v_mov_b32_e32 v13, v131
	v_mov_b32_e32 v14, v132
	v_mov_b32_e32 v15, v133
	v_mov_b32_e32 v16, v134
	v_mov_b32_e32 v17, v135
	v_mov_b32_e32 v18, v136
	v_mov_b32_e32 v19, v137
	v_mov_b32_e32 v20, v138
	v_mov_b32_e32 v21, v139
	v_mov_b32_e32 v22, v140
	v_mov_b32_e32 v23, v141
	v_mov_b32_e32 v24, v142
	v_mov_b32_e32 v25, v143
	v_mov_b32_e32 v26, v144
	v_mov_b32_e32 v27, v145
	v_mov_b32_e32 v28, v146
	v_mov_b32_e32 v29, v147
	v_mov_b32_e32 v30, v148
	v_mov_b32_e32 v31, v149
	v_mov_b32_e32 v32, v150
	v_mov_b32_e32 v33, v151
.Lpfl_w12:
	buffer_load_dwordx4 v[104:107], v182, s[4:7], s92 offen
	buffer_load_dwordx4 v[92:95], v183, s[4:7], s92 offen
	buffer_load_dwordx4 v[112:115], v184, s[4:7], s92 offen
	buffer_load_dwordx4 v[116:119], v185, s[4:7], s92 offen
	buffer_load_dwordx4 v[100:103], v186, s[4:7], s92 offen
	buffer_load_dwordx4 v[108:111], v187, s[4:7], s92 offen
	s_cmp_eq_u32 s67, 0
	s_cbranch_scc1 .Lpfl_nw
	s_waitcnt vmcnt(6)
.Lpfl_nw:
	v_add_u32_e32 v188, 0, v161
	v_mov_b32_e32 v34, 0
	v_add_u32_e32 v189, s29, v172
	s_mov_b32 s2, -2
	v_mov_b32_e32 v35, v34
	v_mov_b32_e32 v36, v34
	v_mov_b32_e32 v37, v34
	v_mov_b32_e32 v38, v34
	v_mov_b32_e32 v39, v34
	v_mov_b32_e32 v40, v34
	v_mov_b32_e32 v41, v34
	v_mov_b32_e32 v42, v34
	v_mov_b32_e32 v43, v34
	v_mov_b32_e32 v44, v34
	v_mov_b32_e32 v45, v34
	v_mov_b32_e32 v46, v34
	v_mov_b32_e32 v47, v34
	v_mov_b32_e32 v48, v34
	v_mov_b32_e32 v49, v34
	v_mov_b32_e32 v50, v34
	v_mov_b32_e32 v51, v34
	v_mov_b32_e32 v120, v34
	v_mov_b32_e32 v121, v34
	v_mov_b32_e32 v122, v34
	v_mov_b32_e32 v123, v34
	v_mov_b32_e32 v124, v34
	v_mov_b32_e32 v125, v34
	v_mov_b32_e32 v126, v34
	v_mov_b32_e32 v127, v34
	v_mov_b32_e32 v128, v34
	v_mov_b32_e32 v129, v34
	v_mov_b32_e32 v130, v34
	v_mov_b32_e32 v131, v34
	v_mov_b32_e32 v132, v34
	v_mov_b32_e32 v133, v34
	v_mov_b32_e32 v134, v34
	v_mov_b32_e32 v135, v34
	v_mov_b32_e32 v136, v34
	v_mov_b32_e32 v137, v34
	v_mov_b32_e32 v138, v34
	v_mov_b32_e32 v139, v34
	v_mov_b32_e32 v140, v34
	v_mov_b32_e32 v141, v34
	v_mov_b32_e32 v142, v34
	v_mov_b32_e32 v143, v34
	v_mov_b32_e32 v144, v34
	v_mov_b32_e32 v145, v34
	v_mov_b32_e32 v146, v34
	v_mov_b32_e32 v147, v34
	v_mov_b32_e32 v148, v34
	v_mov_b32_e32 v149, v34
	v_mov_b32_e32 v150, v34
	v_mov_b32_e32 v151, v34
	v_mov_b32_e32 v152, v34
	v_mov_b32_e32 v153, v34
	v_mov_b32_e32 v154, v34
	v_mov_b32_e32 v155, v34
	s_waitcnt vmcnt(22)
	v_cvt_pk_bf16_f32 v88, v52, v56
	v_cvt_pk_bf16_f32 v52, v53, v57
	s_waitcnt vmcnt(20)
	v_cvt_pk_bf16_f32 v89, v60, v64
	v_cvt_pk_bf16_f32 v53, v61, v65
	v_cvt_pk_bf16_f32 v56, v54, v58
	v_cvt_pk_bf16_f32 v57, v62, v66
	v_cvt_pk_bf16_f32 v54, v55, v59
	v_cvt_pk_bf16_f32 v55, v63, v67
	ds_write2_b64 v188, v[88:89], v[52:53] offset1:16
	ds_write2_b64 v180, v[56:57], v[54:55] offset0:32 offset1:48
	s_waitcnt vmcnt(19)
	ds_write_b128 v189, v[68:71] offset:32768
	s_waitcnt vmcnt(18)
	ds_write_b128 v181, v[72:75] offset:33792
	s_waitcnt vmcnt(17)
	ds_write_b128 v189, v[76:79] offset:34816
	s_waitcnt vmcnt(16)
	ds_write_b128 v181, v[80:83] offset:35840
	s_waitcnt vmcnt(15)
	ds_write_b128 v189, v[84:87] offset:36864
	s_waitcnt vmcnt(14)
	ds_write_b128 v181, v[96:99] offset:37888
	v_mov_b32_e32 v52, v34
	v_mov_b32_e32 v53, v34
	v_mov_b32_e32 v54, v34
	v_mov_b32_e32 v55, v34
	v_mov_b32_e32 v56, v34
	v_mov_b32_e32 v57, v34
	v_mov_b32_e32 v58, v34
	v_mov_b32_e32 v59, v34
	v_mov_b32_e32 v60, v34
	v_mov_b32_e32 v61, v34
	v_mov_b32_e32 v62, v34
	v_mov_b32_e32 v63, v34
	v_mov_b32_e32 v64, v34
	v_mov_b32_e32 v65, v34
	v_mov_b32_e32 v66, v34
	v_mov_b32_e32 v67, v34
	v_mov_b32_e32 v68, v34
	v_mov_b32_e32 v69, v34
	v_mov_b32_e32 v70, v34
	v_mov_b32_e32 v71, v34
	v_mov_b32_e32 v72, v34
	v_mov_b32_e32 v73, v34
	v_mov_b32_e32 v74, v34
	v_mov_b32_e32 v75, v34
	v_mov_b32_e32 v76, v34
	v_mov_b32_e32 v77, v34
	v_mov_b32_e32 v78, v34
	v_mov_b32_e32 v79, v34
	v_mov_b32_e32 v80, v34
	v_mov_b32_e32 v81, v34
	v_mov_b32_e32 v82, v34
	v_mov_b32_e32 v83, v34
	v_mov_b32_e32 v84, v34
	v_mov_b32_e32 v85, v34
	v_mov_b32_e32 v86, v34
	v_mov_b32_e32 v87, v34
	v_mov_b32_e32 v88, v34
	v_mov_b32_e32 v89, v34
	v_mov_b32_e32 v96, v34
	v_mov_b32_e32 v97, v34
	v_mov_b32_e32 v98, v34
	v_mov_b32_e32 v99, v34
	s_waitcnt lgkmcnt(0)
	s_barrier
.Lxl_disp:
	s_mov_b32 s67, 0
	s_sub_i32 s81, s30, s31
	s_add_i32 s82, s80, 0x100
	s_cmp_gt_i32 s81, s82
	s_cbranch_scc1 .LBB0_1785
	s_cmp_eq_u32 s84, 0
	s_cbranch_scc1 .Lmoe_l_b
	s_add_i32 s81, s86, 1
	s_sub_i32 s81, s81, s87
	s_cmp_le_i32 s81, s82
	s_cbranch_scc1 .Lmoe_l_b
